# stack5 = stack4 + half of the GLA in-projection tail conversion items moved to the scan-phase converter
# baseline (speedup 1.0000x reference)
.LBB0_407:
	s_cmpk_lg_i32 s94, 0x100
	s_cselect_b64 s[4:5], -1, 0
	s_cmpk_lt_i32 s90, 0xa4
	s_cselect_b64 s[6:7], -1, 0
	s_or_b64 s[4:5], s[6:7], s[4:5]
	s_and_b64 vcc, exec, s[4:5]
	s_cbranch_vccnz .LBB0_466
	s_add_u32 s2, s84, 0x14b00000
	s_mul_i32 s5, s91, 0x2400
	s_addc_u32 s8, s85, 0
	s_add_i32 s5, s5, 0
	v_and_b32_e32 v2, 7, v0
	s_mul_i32 s4, s90, 24
	v_mul_u32_u24_e32 v4, 0x90, v1
	v_lshrrev_b32_e32 v8, 3, v1
	v_lshl_add_u32 v9, v2, 4, s5
	v_lshlrev_b32_e32 v2, 3, v2
	s_add_u32 s10, s84, 0x4b00000
	s_mov_b32 s9, 0
	s_waitcnt lgkmcnt(0)
	v_mov_b32_e32 v3, 0
	v_mul_u32_u24_e32 v10, 0x90, v8
	v_or_b32_e32 v11, 8, v8
	v_or_b32_e32 v12, 16, v8
	v_or_b32_e32 v13, 24, v8
	v_or_b32_e32 v14, 32, v8
	v_or_b32_e32 v15, 40, v8
	v_or_b32_e32 v16, 48, v8
	v_or_b32_e32 v17, 56, v8
	s_addc_u32 s11, s85, 0
	s_add_i32 s12, s91, s4
	s_addk_i32 s12, 0xf60
	s_movk_i32 s13, 0x4000
	s_movk_i32 s14, 0x800
	s_movk_i32 s15, 0x2000
	s_movk_i32 s16, 0x6000
	s_mov_b32 s17, 0xa000
	s_mov_b32 s18, 0x8000
	s_mov_b32 s19, 0xe000
	s_mov_b32 s20, 0xc000
	s_mov_b32 s21, 0x12000
	s_mov_b32 s22, 0x10000
	s_mov_b32 s23, 0x16000
	s_mov_b32 s24, 0x14000
	s_mov_b32 s25, 0x1a000
	s_mov_b32 s26, 0x18000
	s_mov_b32 s27, 0x1e000
	s_mov_b32 s28, 0x1c000
	s_mov_b32 s29, 0x22000
	s_mov_b32 s30, 0x20000
	s_mov_b32 s31, 0x26000
	s_mov_b32 s33, 0x24000
	s_mov_b32 s34, 0x2a000
	s_mov_b32 s35, 0x28000
	s_mov_b32 s36, 0x2e000
	s_mov_b32 s37, 0x2c000
	s_mov_b32 s38, 0x32000
	s_mov_b32 s39, 0x30000
	s_mov_b32 s40, 0x36000
	s_mov_b32 s41, 0x34000
	s_mov_b32 s42, 0x3a000
	s_mov_b32 s43, 0x38000
	s_mov_b32 s44, 0x3e000
	s_mov_b32 s45, 0x3c000
	v_add_u32_e32 v18, s5, v4
	s_movk_i32 s47, 0x400
	s_mov_b32 s48, 0x3f000
	v_lshlrev_b32_e32 v2, 1, v2
	s_branch .LBB0_411

.LBB0_410:
	s_add_i32 s9, s9, 8
	s_cmp_lg_u32 s9, 24
	s_cbranch_scc0 .LBB0_466

.LBB0_1082:
	s_add_i32 s4, s11, s2
	s_cmpk_gt_i32 s4, 0x23ff
	s_cbranch_scc1 .LBB0_1081
	s_addk_i32 s4, 0xf760
	s_add_i32 s5, s4, 0x2f40
	s_ashr_i32 s6, s5, 31
	s_lshr_b32 s6, s6, 19
	s_add_i32 s5, s5, s6
	s_and_b32 s5, s5, 0xffffe000
	s_add_i32 s6, s4, s5
	s_add_i32 s5, s6, 0x4f40
	s_ashr_i32 s4, s5, 31
	s_lshr_b32 s4, s4, 18
	s_add_i32 s4, s5, s4
	s_and_b32 s4, s4, 0xffffc000
	s_sub_i32 s7, s5, s4
	s_sext_i32_i16 s4, s7
	s_bfe_u32 s4, s4, 0x90016
	s_add_i32 s4, s7, s4
	s_sext_i32_i16 s72, s4
	s_ashr_i32 s4, s72, 9
	s_and_b32 s72, s72, 0xfffffe00
	s_sub_i32 s72, s7, s72
	s_add_i32 s6, s6, 0x8f3f
	s_cmpk_gt_u32 s6, 0x7ffe
	s_mov_b64 s[6:7], -1
	s_cbranch_scc0 .LBB0_1120
	s_and_b32 s5, s5, 0xffffc000
	s_cmpk_lg_i32 s5, 0x4000
	s_cbranch_scc0 .LBB0_1102
	s_ashr_i32 s5, s4, 31
	s_lshl_b64 s[6:7], s[4:5], 23
	s_add_u32 s75, s64, s6
	s_addc_u32 s78, s65, s7
	s_lshl_b64 s[6:7], s[4:5], 22
	s_add_u32 s73, s9, s6
	s_addc_u32 s74, s10, s7
	s_bfe_u32 s5, s72, 0x5001a
	s_add_i32 s5, s72, s5
	s_sext_i32_i16 s5, s5
	s_ashr_i32 s5, s5, 5
	s_lshl_b32 s6, s5, 6
	s_lshl_b32 s5, s5, 11
	s_lshl_b32 s7, s72, 6
	s_sub_i32 s5, s7, s5
	v_or_b32_e32 v4, s5, v1
	s_ashr_i32 s7, s6, 31
	s_lshl_b64 s[76:77], s[6:7], 13
	v_cmp_gt_i32_e32 vcc, s13, v4
	s_add_u32 s76, s75, s76
	s_addc_u32 s77, s78, s77
	v_cndmask_b32_e32 v4, 0, v4, vcc
	v_ashrrev_i32_e32 v5, 31, v4
	v_lshl_add_u64 v[4:5], v[4:5], 2, s[76:77]
	v_add_co_u32_e32 v6, vcc, s14, v4
	s_mov_b32 s75, 0x42000
	s_nop 0
	v_addc_co_u32_e32 v7, vcc, 0, v5, vcc
	global_load_dword v19, v[6:7], off nt
	global_load_dword v20, v[4:5], off nt
	v_add_co_u32_e32 v6, vcc, s15, v4
	s_lshl_b64 s[6:7], s[6:7], 1
	s_nop 0
	v_addc_co_u32_e32 v7, vcc, 0, v5, vcc
	global_load_dword v21, v[6:7], off nt
	v_add_co_u32_e32 v6, vcc, s12, v4
	s_add_u32 s6, s73, s6
	s_nop 0
	v_addc_co_u32_e32 v7, vcc, 0, v5, vcc
	global_load_dword v22, v[6:7], off nt
	v_add_co_u32_e32 v6, vcc, s16, v4
	s_addc_u32 s7, s74, s7
	s_nop 0
	v_addc_co_u32_e32 v7, vcc, 0, v5, vcc
	global_load_dword v23, v[6:7], off nt
	v_add_co_u32_e32 v6, vcc, s17, v4
	s_nop 1
	v_addc_co_u32_e32 v7, vcc, 0, v5, vcc
	global_load_dword v24, v[6:7], off nt
	v_add_co_u32_e32 v6, vcc, s18, v4
	s_nop 1
	v_addc_co_u32_e32 v7, vcc, 0, v5, vcc
	global_load_dword v25, v[6:7], off nt
	v_add_co_u32_e32 v6, vcc, s19, v4
	s_nop 1
	v_addc_co_u32_e32 v7, vcc, 0, v5, vcc
	global_load_dword v26, v[6:7], off nt
	v_add_co_u32_e32 v6, vcc, s8, v4
	s_nop 1
	v_addc_co_u32_e32 v7, vcc, 0, v5, vcc
	global_load_dword v27, v[6:7], off nt
	v_add_co_u32_e32 v6, vcc, s20, v4
	s_nop 1
	v_addc_co_u32_e32 v7, vcc, 0, v5, vcc
	global_load_dword v28, v[6:7], off nt
	v_add_co_u32_e32 v6, vcc, s21, v4
	s_nop 1
	v_addc_co_u32_e32 v7, vcc, 0, v5, vcc
	global_load_dword v29, v[6:7], off nt
	v_add_co_u32_e32 v6, vcc, s22, v4
	s_nop 1
	v_addc_co_u32_e32 v7, vcc, 0, v5, vcc
	global_load_dword v30, v[6:7], off nt
	v_add_co_u32_e32 v6, vcc, s23, v4
	s_nop 1
	v_addc_co_u32_e32 v7, vcc, 0, v5, vcc
	global_load_dword v31, v[6:7], off nt
	v_add_co_u32_e32 v6, vcc, s24, v4
	s_nop 1
	v_addc_co_u32_e32 v7, vcc, 0, v5, vcc
	global_load_dword v32, v[6:7], off nt
	v_add_co_u32_e32 v6, vcc, s25, v4
	s_nop 1
	v_addc_co_u32_e32 v7, vcc, 0, v5, vcc
	global_load_dword v33, v[6:7], off nt
	v_add_co_u32_e32 v6, vcc, s26, v4
	s_nop 1
	v_addc_co_u32_e32 v7, vcc, 0, v5, vcc
	global_load_dword v34, v[6:7], off nt
	v_add_co_u32_e32 v6, vcc, s27, v4
	s_nop 1
	v_addc_co_u32_e32 v7, vcc, 0, v5, vcc
	global_load_dword v35, v[6:7], off nt
	v_add_co_u32_e32 v6, vcc, s28, v4
	s_nop 1
	v_addc_co_u32_e32 v7, vcc, 0, v5, vcc
	global_load_dword v36, v[6:7], off nt
	v_add_co_u32_e32 v6, vcc, s29, v4
	s_nop 1
	v_addc_co_u32_e32 v7, vcc, 0, v5, vcc
	global_load_dword v37, v[6:7], off nt
	v_add_co_u32_e32 v6, vcc, s30, v4
	s_nop 1
	v_addc_co_u32_e32 v7, vcc, 0, v5, vcc
	global_load_dword v38, v[6:7], off nt
	v_add_co_u32_e32 v6, vcc, s31, v4
	s_nop 1
	v_addc_co_u32_e32 v7, vcc, 0, v5, vcc
	global_load_dword v39, v[6:7], off nt
	v_add_co_u32_e32 v6, vcc, s33, v4
	s_nop 1
	v_addc_co_u32_e32 v7, vcc, 0, v5, vcc
	global_load_dword v40, v[6:7], off nt
	v_add_co_u32_e32 v6, vcc, s36, v4
	s_nop 1
	v_addc_co_u32_e32 v7, vcc, 0, v5, vcc
	global_load_dword v41, v[6:7], off nt
	v_add_co_u32_e32 v6, vcc, s37, v4
	s_nop 1
	v_addc_co_u32_e32 v7, vcc, 0, v5, vcc
	global_load_dword v42, v[6:7], off nt
	v_add_co_u32_e32 v6, vcc, s38, v4
	s_nop 1
	v_addc_co_u32_e32 v7, vcc, 0, v5, vcc
	global_load_dword v43, v[6:7], off nt
	v_add_co_u32_e32 v6, vcc, s39, v4
	s_nop 1
	v_addc_co_u32_e32 v7, vcc, 0, v5, vcc
	global_load_dword v44, v[6:7], off nt
	v_add_co_u32_e32 v6, vcc, s40, v4
	s_nop 1
	v_addc_co_u32_e32 v7, vcc, 0, v5, vcc
	global_load_dword v45, v[6:7], off nt
	v_add_co_u32_e32 v6, vcc, s41, v4
	s_nop 1
	v_addc_co_u32_e32 v7, vcc, 0, v5, vcc
	global_load_dword v46, v[6:7], off nt
	v_add_co_u32_e32 v6, vcc, s42, v4
	s_nop 1
	v_addc_co_u32_e32 v7, vcc, 0, v5, vcc
	global_load_dword v47, v[6:7], off nt
	v_add_co_u32_e32 v6, vcc, s43, v4
	s_nop 1
	v_addc_co_u32_e32 v7, vcc, 0, v5, vcc
	global_load_dword v48, v[6:7], off nt
	v_add_co_u32_e32 v6, vcc, s44, v4
	s_nop 1
	v_addc_co_u32_e32 v7, vcc, 0, v5, vcc
	global_load_dword v49, v[6:7], off nt
	v_add_co_u32_e32 v6, vcc, s45, v4
	s_nop 1
	v_addc_co_u32_e32 v7, vcc, 0, v5, vcc
	global_load_dword v50, v[6:7], off nt
	v_add_co_u32_e32 v6, vcc, s75, v4
	s_mov_b32 s75, 0x40000
	s_nop 0
	v_addc_co_u32_e32 v7, vcc, 0, v5, vcc
	global_load_dword v51, v[6:7], off nt
	v_add_co_u32_e32 v6, vcc, s75, v4
	s_mov_b32 s75, 0x46000
	s_nop 0
	v_addc_co_u32_e32 v7, vcc, 0, v5, vcc
	global_load_dword v52, v[6:7], off nt
	v_add_co_u32_e32 v6, vcc, s75, v4
	s_mov_b32 s75, 0x44000
	s_nop 0
	v_addc_co_u32_e32 v7, vcc, 0, v5, vcc
	global_load_dword v53, v[6:7], off nt
	v_add_co_u32_e32 v6, vcc, s75, v4
	s_mov_b32 s75, 0x4a000
	s_nop 0
	v_addc_co_u32_e32 v7, vcc, 0, v5, vcc
	global_load_dword v54, v[6:7], off nt
	v_add_co_u32_e32 v6, vcc, s75, v4
	s_mov_b32 s75, 0x48000
	s_nop 0
	v_addc_co_u32_e32 v7, vcc, 0, v5, vcc
	global_load_dword v55, v[6:7], off nt
	v_add_co_u32_e32 v6, vcc, s75, v4
	s_mov_b32 s75, 0x4e000
	s_nop 0
	v_addc_co_u32_e32 v7, vcc, 0, v5, vcc
	global_load_dword v56, v[6:7], off nt
	v_add_co_u32_e32 v6, vcc, s75, v4
	s_mov_b32 s75, 0x4c000
	s_nop 0
	v_addc_co_u32_e32 v7, vcc, 0, v5, vcc
	global_load_dword v57, v[6:7], off nt
	v_add_co_u32_e32 v6, vcc, s75, v4
	s_mov_b32 s75, 0x52000
	s_nop 0
	v_addc_co_u32_e32 v7, vcc, 0, v5, vcc
	global_load_dword v58, v[6:7], off nt
	v_add_co_u32_e32 v6, vcc, s75, v4
	s_mov_b32 s75, 0x50000
	s_nop 0
	v_addc_co_u32_e32 v7, vcc, 0, v5, vcc
	global_load_dword v59, v[6:7], off nt
	v_add_co_u32_e32 v6, vcc, s75, v4
	s_mov_b32 s75, 0x56000
	s_nop 0
	v_addc_co_u32_e32 v7, vcc, 0, v5, vcc
	global_load_dword v60, v[6:7], off nt
	v_add_co_u32_e32 v6, vcc, s75, v4
	s_mov_b32 s75, 0x54000
	s_nop 0
	v_addc_co_u32_e32 v7, vcc, 0, v5, vcc
	global_load_dword v61, v[6:7], off nt
	v_add_co_u32_e32 v6, vcc, s75, v4
	s_mov_b32 s75, 0x5a000
	s_nop 0
	v_addc_co_u32_e32 v7, vcc, 0, v5, vcc
	global_load_dword v62, v[6:7], off nt
	v_add_co_u32_e32 v6, vcc, s75, v4
	s_mov_b32 s75, 0x58000
	s_nop 0
	v_addc_co_u32_e32 v7, vcc, 0, v5, vcc
	global_load_dword v63, v[6:7], off nt
	v_add_co_u32_e32 v6, vcc, s75, v4
	s_mov_b32 s75, 0x5e000
	s_nop 0
	v_addc_co_u32_e32 v7, vcc, 0, v5, vcc
	global_load_dword v64, v[6:7], off nt
	v_add_co_u32_e32 v6, vcc, s75, v4
	s_mov_b32 s75, 0x5c000
	s_nop 0
	v_addc_co_u32_e32 v7, vcc, 0, v5, vcc
	global_load_dword v65, v[6:7], off nt
	v_add_co_u32_e32 v6, vcc, s75, v4
	s_mov_b32 s75, 0x62000
	s_nop 0
	v_addc_co_u32_e32 v7, vcc, 0, v5, vcc
	global_load_dword v66, v[6:7], off nt
	v_add_co_u32_e32 v6, vcc, s75, v4
	s_nop 1
	v_addc_co_u32_e32 v7, vcc, 0, v5, vcc
	global_load_dword v67, v[6:7], off nt
	v_add_co_u32_e32 v6, vcc, s47, v4
	s_nop 1
	v_addc_co_u32_e32 v7, vcc, 0, v5, vcc
	global_load_dword v68, v[6:7], off nt
	v_add_co_u32_e32 v6, vcc, s48, v4
	s_nop 1
	v_addc_co_u32_e32 v7, vcc, 0, v5, vcc
	global_load_dword v69, v[6:7], off nt
	v_add_co_u32_e32 v6, vcc, s49, v4
	s_nop 1
	v_addc_co_u32_e32 v7, vcc, 0, v5, vcc
	global_load_dword v70, v[6:7], off nt
	v_add_co_u32_e32 v6, vcc, s50, v4
	s_nop 1
	v_addc_co_u32_e32 v7, vcc, 0, v5, vcc
	global_load_dword v71, v[6:7], off nt
	v_add_co_u32_e32 v6, vcc, s51, v4
	s_nop 1
	v_addc_co_u32_e32 v7, vcc, 0, v5, vcc
	global_load_dword v72, v[6:7], off nt
	v_add_co_u32_e32 v6, vcc, s52, v4
	s_nop 1
	v_addc_co_u32_e32 v7, vcc, 0, v5, vcc
	global_load_dword v73, v[6:7], off nt
	v_add_co_u32_e32 v6, vcc, s53, v4
	s_nop 1
	v_addc_co_u32_e32 v7, vcc, 0, v5, vcc
	global_load_dword v74, v[6:7], off nt
	v_add_co_u32_e32 v6, vcc, s54, v4
	s_nop 1
	v_addc_co_u32_e32 v7, vcc, 0, v5, vcc
	global_load_dword v75, v[6:7], off nt
	v_add_co_u32_e32 v6, vcc, s55, v4
	s_nop 1
	v_addc_co_u32_e32 v7, vcc, 0, v5, vcc
	global_load_dword v76, v[6:7], off nt
	v_add_co_u32_e32 v6, vcc, s56, v4
	s_nop 1
	v_addc_co_u32_e32 v7, vcc, 0, v5, vcc
	global_load_dword v77, v[6:7], off nt
	v_add_co_u32_e32 v6, vcc, s57, v4
	s_nop 1
	v_addc_co_u32_e32 v7, vcc, 0, v5, vcc
	global_load_dword v78, v[6:7], off nt
	v_add_co_u32_e32 v6, vcc, s58, v4
	s_nop 1
	v_addc_co_u32_e32 v7, vcc, 0, v5, vcc
	global_load_dword v79, v[6:7], off nt
	v_add_co_u32_e32 v6, vcc, s59, v4
	s_nop 1
	v_addc_co_u32_e32 v7, vcc, 0, v5, vcc
	global_load_dword v80, v[6:7], off nt
	v_add_co_u32_e32 v6, vcc, s68, v4
	s_nop 1
	v_addc_co_u32_e32 v7, vcc, 0, v5, vcc
	v_add_co_u32_e32 v4, vcc, s69, v4
	global_load_dword v81, v[6:7], off nt
	s_nop 0
	v_addc_co_u32_e32 v5, vcc, 0, v5, vcc
	global_load_dword v82, v[4:5], off nt
	s_waitcnt vmcnt(62)
	v_cvt_pk_bf16_f32 v4, v20, v19
	s_waitcnt vmcnt(60)
	v_cvt_pk_bf16_f32 v5, v22, v21
	s_waitcnt vmcnt(58)
	v_cvt_pk_bf16_f32 v6, v24, v23
	s_waitcnt vmcnt(56)
	v_cvt_pk_bf16_f32 v7, v26, v25
	ds_write_b128 v18, v[4:7]
	s_waitcnt vmcnt(54)
	v_cvt_pk_bf16_f32 v4, v28, v27
	s_waitcnt vmcnt(52)
	v_cvt_pk_bf16_f32 v5, v30, v29
	s_waitcnt vmcnt(50)
	v_cvt_pk_bf16_f32 v6, v32, v31
	s_waitcnt vmcnt(48)
	v_cvt_pk_bf16_f32 v7, v34, v33
	ds_write_b128 v18, v[4:7] offset:16
	s_waitcnt vmcnt(46)
	v_cvt_pk_bf16_f32 v4, v36, v35
	s_waitcnt vmcnt(44)
	v_cvt_pk_bf16_f32 v5, v38, v37
	s_waitcnt vmcnt(42)
	v_cvt_pk_bf16_f32 v6, v40, v39
	s_waitcnt vmcnt(40)
	v_cvt_pk_bf16_f32 v7, v42, v41
	ds_write_b128 v18, v[4:7] offset:32
	s_waitcnt vmcnt(38)
	v_cvt_pk_bf16_f32 v4, v44, v43
	s_waitcnt vmcnt(36)
	v_cvt_pk_bf16_f32 v5, v46, v45
	s_waitcnt vmcnt(34)
	v_cvt_pk_bf16_f32 v6, v48, v47
	s_waitcnt vmcnt(32)
	v_cvt_pk_bf16_f32 v7, v50, v49
	ds_write_b128 v18, v[4:7] offset:48
	s_waitcnt vmcnt(30)
	v_cvt_pk_bf16_f32 v4, v52, v51
	s_waitcnt vmcnt(28)
	v_cvt_pk_bf16_f32 v5, v54, v53
	s_waitcnt vmcnt(26)
	v_cvt_pk_bf16_f32 v6, v56, v55
	s_waitcnt vmcnt(24)
	v_cvt_pk_bf16_f32 v7, v58, v57
	ds_write_b128 v18, v[4:7] offset:64
	s_waitcnt vmcnt(22)
	v_cvt_pk_bf16_f32 v4, v60, v59
	s_waitcnt vmcnt(20)
	v_cvt_pk_bf16_f32 v5, v62, v61
	s_waitcnt vmcnt(18)
	v_cvt_pk_bf16_f32 v6, v64, v63
	s_waitcnt vmcnt(16)
	v_cvt_pk_bf16_f32 v7, v66, v65
	ds_write_b128 v18, v[4:7] offset:80
	s_waitcnt vmcnt(14)
	v_cvt_pk_bf16_f32 v4, v68, v67
	s_waitcnt vmcnt(12)
	v_cvt_pk_bf16_f32 v5, v70, v69
	s_waitcnt vmcnt(10)
	v_cvt_pk_bf16_f32 v6, v72, v71
	s_waitcnt vmcnt(8)
	v_cvt_pk_bf16_f32 v7, v74, v73
	ds_write_b128 v18, v[4:7] offset:96
	s_waitcnt vmcnt(6)
	v_cvt_pk_bf16_f32 v4, v76, v75
	s_waitcnt vmcnt(4)
	v_cvt_pk_bf16_f32 v5, v78, v77
	s_waitcnt vmcnt(2)
	v_cvt_pk_bf16_f32 v6, v80, v79
	s_waitcnt vmcnt(0)
	v_cvt_pk_bf16_f32 v7, v82, v81
	ds_write_b128 v18, v[4:7] offset:112
	s_waitcnt lgkmcnt(0)
	v_or_b32_e32 v6, s5, v8
	v_lshl_add_u64 v[4:5], s[6:7], 0, v[2:3]
	v_cmp_gt_i32_e32 vcc, s13, v6
	s_and_saveexec_b64 s[6:7], vcc
	s_cbranch_execz .LBB0_1087
	v_add_u32_e32 v7, v9, v10
	ds_read_b128 v[20:23], v7
	v_ashrrev_i32_e32 v7, 31, v6
	v_lshlrev_b64 v[6:7], 11, v[6:7]
	v_lshl_add_u64 v[6:7], v[4:5], 0, v[6:7]
	s_waitcnt lgkmcnt(0)
	global_store_dwordx4 v[6:7], v[20:23], off nt

.LBB0_1248:
	s_add_i32 s8, s71, s8
	s_cmpk_gt_i32 s8, 0x23ff
	s_cbranch_scc1 .LBB0_1247
	s_addk_i32 s8, 0x26a0
	s_ashr_i32 s9, s8, 31
	s_lshr_b32 s9, s9, 19
	s_add_i32 s9, s8, s9
	s_and_b32 s10, s9, 0xffffe000
	s_lshl_b32 s9, s9, 1
	s_sub_i32 s8, s8, s10
	s_and_b32 s9, s9, 0xffffc000
	s_add_i32 s10, s8, s9
	s_add_i32 s9, s10, 0x2000
	s_ashr_i32 s8, s9, 31
	s_lshr_b32 s8, s8, 18
	s_add_i32 s8, s9, s8
	s_and_b32 s8, s8, 0xffffc000
	s_sub_i32 s11, s9, s8
	s_sext_i32_i16 s8, s11
	s_bfe_u32 s8, s8, 0x90016
	s_add_i32 s8, s11, s8
	s_sext_i32_i16 s72, s8
	s_ashr_i32 s8, s72, 9
	s_and_b32 s72, s72, 0xfffffe00
	s_sub_i32 s72, s11, s72
	s_addk_i32 s10, 0x5fff
	s_cmpk_gt_u32 s10, 0x7ffe
	s_mov_b64 s[10:11], -1
	s_cbranch_scc0 .LBB0_1286
	s_and_b32 s9, s9, 0xffffc000
	s_cmpk_lg_i32 s9, 0x4000
	s_cbranch_scc0 .LBB0_1268
	s_ashr_i32 s9, s8, 31
	s_lshl_b64 s[10:11], s[8:9], 23
	s_add_u32 s75, s64, s10
	s_addc_u32 s78, s65, s11
	s_lshl_b64 s[10:11], s[8:9], 22
	s_add_u32 s73, s2, s10
	s_addc_u32 s74, s33, s11
	s_bfe_u32 s9, s72, 0x5001a
	s_add_i32 s9, s72, s9
	s_sext_i32_i16 s9, s9
	s_ashr_i32 s9, s9, 5
	s_lshl_b32 s10, s9, 6
	s_lshl_b32 s9, s9, 11
	s_lshl_b32 s11, s72, 6
	s_sub_i32 s9, s11, s9
	v_or_b32_e32 v4, s9, v1
	s_ashr_i32 s11, s10, 31
	s_lshl_b64 s[76:77], s[10:11], 13
	v_cmp_gt_i32_e32 vcc, s19, v4
	s_add_u32 s76, s75, s76
	s_addc_u32 s77, s78, s77
	v_cndmask_b32_e32 v4, 0, v4, vcc
	v_ashrrev_i32_e32 v5, 31, v4
	v_lshl_add_u64 v[4:5], v[4:5], 2, s[76:77]
	v_add_co_u32_e32 v6, vcc, s17, v4
	s_mov_b32 s75, 0x42000
	s_nop 0
	v_addc_co_u32_e32 v7, vcc, 0, v5, vcc
	global_load_dword v20, v[6:7], off nt
	global_load_dword v21, v[4:5], off nt
	v_add_co_u32_e32 v6, vcc, s20, v4
	s_lshl_b64 s[10:11], s[10:11], 1
	s_nop 0
	v_addc_co_u32_e32 v7, vcc, 0, v5, vcc
	global_load_dword v22, v[6:7], off nt
	v_add_co_u32_e32 v6, vcc, s18, v4
	s_add_u32 s10, s73, s10
	s_nop 0
	v_addc_co_u32_e32 v7, vcc, 0, v5, vcc
	global_load_dword v23, v[6:7], off nt
	v_add_co_u32_e32 v6, vcc, s21, v4
	s_addc_u32 s11, s74, s11
	s_nop 0
	v_addc_co_u32_e32 v7, vcc, 0, v5, vcc
	global_load_dword v24, v[6:7], off nt
	v_add_co_u32_e32 v6, vcc, s22, v4
	s_nop 1
	v_addc_co_u32_e32 v7, vcc, 0, v5, vcc
	global_load_dword v25, v[6:7], off nt
	v_add_co_u32_e32 v6, vcc, s23, v4
	s_nop 1
	v_addc_co_u32_e32 v7, vcc, 0, v5, vcc
	global_load_dword v26, v[6:7], off nt
	v_add_co_u32_e32 v6, vcc, s24, v4
	s_nop 1
	v_addc_co_u32_e32 v7, vcc, 0, v5, vcc
	global_load_dword v27, v[6:7], off nt
	v_add_co_u32_e32 v6, vcc, s15, v4
	s_nop 1
	v_addc_co_u32_e32 v7, vcc, 0, v5, vcc
	global_load_dword v28, v[6:7], off nt
	v_add_co_u32_e32 v6, vcc, s25, v4
	s_nop 1
	v_addc_co_u32_e32 v7, vcc, 0, v5, vcc
	global_load_dword v29, v[6:7], off nt
	v_add_co_u32_e32 v6, vcc, s26, v4
	s_nop 1
	v_addc_co_u32_e32 v7, vcc, 0, v5, vcc
	global_load_dword v30, v[6:7], off nt
	v_add_co_u32_e32 v6, vcc, s27, v4
	s_nop 1
	v_addc_co_u32_e32 v7, vcc, 0, v5, vcc
	global_load_dword v31, v[6:7], off nt
	v_add_co_u32_e32 v6, vcc, s28, v4
	s_nop 1
	v_addc_co_u32_e32 v7, vcc, 0, v5, vcc
	global_load_dword v32, v[6:7], off nt
	v_add_co_u32_e32 v6, vcc, s29, v4
	s_nop 1
	v_addc_co_u32_e32 v7, vcc, 0, v5, vcc
	global_load_dword v33, v[6:7], off nt
	v_add_co_u32_e32 v6, vcc, s30, v4
	s_nop 1
	v_addc_co_u32_e32 v7, vcc, 0, v5, vcc
	global_load_dword v34, v[6:7], off nt
	v_add_co_u32_e32 v6, vcc, s31, v4
	s_nop 1
	v_addc_co_u32_e32 v7, vcc, 0, v5, vcc
	global_load_dword v35, v[6:7], off nt
	v_add_co_u32_e32 v6, vcc, s34, v4
	s_nop 1
	v_addc_co_u32_e32 v7, vcc, 0, v5, vcc
	global_load_dword v36, v[6:7], off nt
	v_add_co_u32_e32 v6, vcc, s35, v4
	s_nop 1
	v_addc_co_u32_e32 v7, vcc, 0, v5, vcc
	global_load_dword v37, v[6:7], off nt
	v_add_co_u32_e32 v6, vcc, s36, v4
	s_nop 1
	v_addc_co_u32_e32 v7, vcc, 0, v5, vcc
	global_load_dword v38, v[6:7], off nt
	v_add_co_u32_e32 v6, vcc, s37, v4
	s_nop 1
	v_addc_co_u32_e32 v7, vcc, 0, v5, vcc
	global_load_dword v39, v[6:7], off nt
	v_add_co_u32_e32 v6, vcc, s38, v4
	s_nop 1
	v_addc_co_u32_e32 v7, vcc, 0, v5, vcc
	global_load_dword v40, v[6:7], off nt
	v_add_co_u32_e32 v6, vcc, s39, v4
	s_nop 1
	v_addc_co_u32_e32 v7, vcc, 0, v5, vcc
	global_load_dword v41, v[6:7], off nt
	v_add_co_u32_e32 v6, vcc, s40, v4
	s_nop 1
	v_addc_co_u32_e32 v7, vcc, 0, v5, vcc
	global_load_dword v42, v[6:7], off nt
	v_add_co_u32_e32 v6, vcc, s41, v4
	s_nop 1
	v_addc_co_u32_e32 v7, vcc, 0, v5, vcc
	global_load_dword v43, v[6:7], off nt
	v_add_co_u32_e32 v6, vcc, s42, v4
	s_nop 1
	v_addc_co_u32_e32 v7, vcc, 0, v5, vcc
	global_load_dword v44, v[6:7], off nt
	v_add_co_u32_e32 v6, vcc, s43, v4
	s_nop 1
	v_addc_co_u32_e32 v7, vcc, 0, v5, vcc
	global_load_dword v45, v[6:7], off nt
	v_add_co_u32_e32 v6, vcc, s44, v4
	s_nop 1
	v_addc_co_u32_e32 v7, vcc, 0, v5, vcc
	global_load_dword v46, v[6:7], off nt
	v_add_co_u32_e32 v6, vcc, s45, v4
	s_nop 1
	v_addc_co_u32_e32 v7, vcc, 0, v5, vcc
	global_load_dword v47, v[6:7], off nt
	v_add_co_u32_e32 v6, vcc, s47, v4
	s_nop 1
	v_addc_co_u32_e32 v7, vcc, 0, v5, vcc
	global_load_dword v48, v[6:7], off nt
	v_add_co_u32_e32 v6, vcc, s48, v4
	s_nop 1
	v_addc_co_u32_e32 v7, vcc, 0, v5, vcc
	global_load_dword v49, v[6:7], off nt
	v_add_co_u32_e32 v6, vcc, s49, v4
	s_nop 1
	v_addc_co_u32_e32 v7, vcc, 0, v5, vcc
	global_load_dword v50, v[6:7], off nt
	v_add_co_u32_e32 v6, vcc, s50, v4
	s_nop 1
	v_addc_co_u32_e32 v7, vcc, 0, v5, vcc
	global_load_dword v51, v[6:7], off nt
	v_add_co_u32_e32 v6, vcc, s75, v4
	s_mov_b32 s75, 0x40000
	s_nop 0
	v_addc_co_u32_e32 v7, vcc, 0, v5, vcc
	global_load_dword v52, v[6:7], off nt
	v_add_co_u32_e32 v6, vcc, s75, v4
	s_mov_b32 s75, 0x46000
	s_nop 0
	v_addc_co_u32_e32 v7, vcc, 0, v5, vcc
	global_load_dword v53, v[6:7], off nt
	v_add_co_u32_e32 v6, vcc, s75, v4
	s_mov_b32 s75, 0x44000
	s_nop 0
	v_addc_co_u32_e32 v7, vcc, 0, v5, vcc
	global_load_dword v54, v[6:7], off nt
	v_add_co_u32_e32 v6, vcc, s75, v4
	s_mov_b32 s75, 0x4a000
	s_nop 0
	v_addc_co_u32_e32 v7, vcc, 0, v5, vcc
	global_load_dword v55, v[6:7], off nt
	v_add_co_u32_e32 v6, vcc, s75, v4
	s_mov_b32 s75, 0x48000
	s_nop 0
	v_addc_co_u32_e32 v7, vcc, 0, v5, vcc
	global_load_dword v56, v[6:7], off nt
	v_add_co_u32_e32 v6, vcc, s75, v4
	s_mov_b32 s75, 0x4e000
	s_nop 0
	v_addc_co_u32_e32 v7, vcc, 0, v5, vcc
	global_load_dword v57, v[6:7], off nt
	v_add_co_u32_e32 v6, vcc, s75, v4
	s_mov_b32 s75, 0x4c000
	s_nop 0
	v_addc_co_u32_e32 v7, vcc, 0, v5, vcc
	global_load_dword v58, v[6:7], off nt
	v_add_co_u32_e32 v6, vcc, s75, v4
	s_mov_b32 s75, 0x52000
	s_nop 0
	v_addc_co_u32_e32 v7, vcc, 0, v5, vcc
	global_load_dword v59, v[6:7], off nt
	v_add_co_u32_e32 v6, vcc, s75, v4
	s_mov_b32 s75, 0x50000
	s_nop 0
	v_addc_co_u32_e32 v7, vcc, 0, v5, vcc
	global_load_dword v60, v[6:7], off nt
	v_add_co_u32_e32 v6, vcc, s75, v4
	s_mov_b32 s75, 0x56000
	s_nop 0
	v_addc_co_u32_e32 v7, vcc, 0, v5, vcc
	global_load_dword v61, v[6:7], off nt
	v_add_co_u32_e32 v6, vcc, s75, v4
	s_mov_b32 s75, 0x54000
	s_nop 0
	v_addc_co_u32_e32 v7, vcc, 0, v5, vcc
	global_load_dword v62, v[6:7], off nt
	v_add_co_u32_e32 v6, vcc, s75, v4
	s_mov_b32 s75, 0x5a000
	s_nop 0
	v_addc_co_u32_e32 v7, vcc, 0, v5, vcc
	global_load_dword v63, v[6:7], off nt
	v_add_co_u32_e32 v6, vcc, s75, v4
	s_mov_b32 s75, 0x58000
	s_nop 0
	v_addc_co_u32_e32 v7, vcc, 0, v5, vcc
	global_load_dword v64, v[6:7], off nt
	v_add_co_u32_e32 v6, vcc, s75, v4
	s_mov_b32 s75, 0x5e000
	s_nop 0
	v_addc_co_u32_e32 v7, vcc, 0, v5, vcc
	global_load_dword v65, v[6:7], off nt
	v_add_co_u32_e32 v6, vcc, s75, v4
	s_mov_b32 s75, 0x5c000
	s_nop 0
	v_addc_co_u32_e32 v7, vcc, 0, v5, vcc
	global_load_dword v66, v[6:7], off nt
	v_add_co_u32_e32 v6, vcc, s75, v4
	s_mov_b32 s75, 0x62000
	s_nop 0
	v_addc_co_u32_e32 v7, vcc, 0, v5, vcc
	global_load_dword v67, v[6:7], off nt
	v_add_co_u32_e32 v6, vcc, s75, v4
	s_mov_b32 s75, 0x60000
	s_nop 0
	v_addc_co_u32_e32 v7, vcc, 0, v5, vcc
	global_load_dword v68, v[6:7], off nt
	v_add_co_u32_e32 v6, vcc, s75, v4
	s_mov_b32 s75, 0x66000
	s_nop 0
	v_addc_co_u32_e32 v7, vcc, 0, v5, vcc
	global_load_dword v69, v[6:7], off nt
	v_add_co_u32_e32 v6, vcc, s75, v4
	s_mov_b32 s75, 0x64000
	s_nop 0
	v_addc_co_u32_e32 v7, vcc, 0, v5, vcc
	global_load_dword v70, v[6:7], off nt
	v_add_co_u32_e32 v6, vcc, s75, v4
	s_mov_b32 s75, 0x6a000
	s_nop 0
	v_addc_co_u32_e32 v7, vcc, 0, v5, vcc
	global_load_dword v71, v[6:7], off nt
	v_add_co_u32_e32 v6, vcc, s75, v4
	s_mov_b32 s75, 0x68000
	s_nop 0
	v_addc_co_u32_e32 v7, vcc, 0, v5, vcc
	global_load_dword v72, v[6:7], off nt
	v_add_co_u32_e32 v6, vcc, s75, v4
	s_nop 1
	v_addc_co_u32_e32 v7, vcc, 0, v5, vcc
	global_load_dword v73, v[6:7], off nt
	v_add_co_u32_e32 v6, vcc, s51, v4
	s_nop 1
	v_addc_co_u32_e32 v7, vcc, 0, v5, vcc
	global_load_dword v74, v[6:7], off nt
	v_add_co_u32_e32 v6, vcc, s52, v4
	s_nop 1
	v_addc_co_u32_e32 v7, vcc, 0, v5, vcc
	global_load_dword v75, v[6:7], off nt
	v_add_co_u32_e32 v6, vcc, s53, v4
	s_nop 1
	v_addc_co_u32_e32 v7, vcc, 0, v5, vcc
	global_load_dword v76, v[6:7], off nt
	v_add_co_u32_e32 v6, vcc, s54, v4
	s_nop 1
	v_addc_co_u32_e32 v7, vcc, 0, v5, vcc
	global_load_dword v77, v[6:7], off nt
	v_add_co_u32_e32 v6, vcc, s55, v4
	s_nop 1
	v_addc_co_u32_e32 v7, vcc, 0, v5, vcc
	global_load_dword v78, v[6:7], off nt
	v_add_co_u32_e32 v6, vcc, s56, v4
	s_nop 1
	v_addc_co_u32_e32 v7, vcc, 0, v5, vcc
	global_load_dword v79, v[6:7], off nt
	v_add_co_u32_e32 v6, vcc, s57, v4
	s_nop 1
	v_addc_co_u32_e32 v7, vcc, 0, v5, vcc
	global_load_dword v80, v[6:7], off nt
	v_add_co_u32_e32 v6, vcc, s58, v4
	s_nop 1
	v_addc_co_u32_e32 v7, vcc, 0, v5, vcc
	global_load_dword v81, v[6:7], off nt
	v_add_co_u32_e32 v6, vcc, s59, v4
	s_nop 1
	v_addc_co_u32_e32 v7, vcc, 0, v5, vcc
	v_add_co_u32_e32 v4, vcc, s68, v4
	global_load_dword v82, v[6:7], off nt
	s_nop 0
	v_addc_co_u32_e32 v5, vcc, 0, v5, vcc
	global_load_dword v83, v[4:5], off nt
	s_waitcnt vmcnt(62)
	v_cvt_pk_bf16_f32 v4, v21, v20
	s_waitcnt vmcnt(60)
	v_cvt_pk_bf16_f32 v5, v23, v22
	s_waitcnt vmcnt(58)
	v_cvt_pk_bf16_f32 v6, v25, v24
	s_waitcnt vmcnt(56)
	v_cvt_pk_bf16_f32 v7, v27, v26
	ds_write_b128 v19, v[4:7]
	s_waitcnt vmcnt(54)
	v_cvt_pk_bf16_f32 v4, v29, v28
	s_waitcnt vmcnt(52)
	v_cvt_pk_bf16_f32 v5, v31, v30
	s_waitcnt vmcnt(50)
	v_cvt_pk_bf16_f32 v6, v33, v32
	s_waitcnt vmcnt(48)
	v_cvt_pk_bf16_f32 v7, v35, v34
	ds_write_b128 v19, v[4:7] offset:16
	s_waitcnt vmcnt(46)
	v_cvt_pk_bf16_f32 v4, v37, v36
	s_waitcnt vmcnt(44)
	v_cvt_pk_bf16_f32 v5, v39, v38
	s_waitcnt vmcnt(42)
	v_cvt_pk_bf16_f32 v6, v41, v40
	s_waitcnt vmcnt(40)
	v_cvt_pk_bf16_f32 v7, v43, v42
	ds_write_b128 v19, v[4:7] offset:32
	s_waitcnt vmcnt(38)
	v_cvt_pk_bf16_f32 v4, v45, v44
	s_waitcnt vmcnt(36)
	v_cvt_pk_bf16_f32 v5, v47, v46
	s_waitcnt vmcnt(34)
	v_cvt_pk_bf16_f32 v6, v49, v48
	s_waitcnt vmcnt(32)
	v_cvt_pk_bf16_f32 v7, v51, v50
	ds_write_b128 v19, v[4:7] offset:48
	s_waitcnt vmcnt(30)
	v_cvt_pk_bf16_f32 v4, v53, v52
	s_waitcnt vmcnt(28)
	v_cvt_pk_bf16_f32 v5, v55, v54
	s_waitcnt vmcnt(26)
	v_cvt_pk_bf16_f32 v6, v57, v56
	s_waitcnt vmcnt(24)
	v_cvt_pk_bf16_f32 v7, v59, v58
	ds_write_b128 v19, v[4:7] offset:64
	s_waitcnt vmcnt(22)
	v_cvt_pk_bf16_f32 v4, v61, v60
	s_waitcnt vmcnt(20)
	v_cvt_pk_bf16_f32 v5, v63, v62
	s_waitcnt vmcnt(18)
	v_cvt_pk_bf16_f32 v6, v65, v64
	s_waitcnt vmcnt(16)
	v_cvt_pk_bf16_f32 v7, v67, v66
	ds_write_b128 v19, v[4:7] offset:80
	s_waitcnt vmcnt(14)
	v_cvt_pk_bf16_f32 v4, v69, v68
	s_waitcnt vmcnt(12)
	v_cvt_pk_bf16_f32 v5, v71, v70
	s_waitcnt vmcnt(10)
	v_cvt_pk_bf16_f32 v6, v73, v72
	s_waitcnt vmcnt(8)
	v_cvt_pk_bf16_f32 v7, v75, v74
	ds_write_b128 v19, v[4:7] offset:96
	s_waitcnt vmcnt(6)
	v_cvt_pk_bf16_f32 v4, v77, v76
	s_waitcnt vmcnt(4)
	v_cvt_pk_bf16_f32 v5, v79, v78
	s_waitcnt vmcnt(2)
	v_cvt_pk_bf16_f32 v6, v81, v80
	s_waitcnt vmcnt(0)
	v_cvt_pk_bf16_f32 v7, v83, v82
	ds_write_b128 v19, v[4:7] offset:112
	s_waitcnt lgkmcnt(0)
	v_or_b32_e32 v6, s9, v8
	v_lshl_add_u64 v[4:5], s[10:11], 0, v[2:3]
	v_cmp_gt_i32_e32 vcc, s19, v6
	s_and_saveexec_b64 s[10:11], vcc
	s_cbranch_execz .LBB0_1253
	v_add_u32_e32 v7, v9, v10
	ds_read_b128 v[20:23], v7
	v_ashrrev_i32_e32 v7, 31, v6
	v_lshlrev_b64 v[6:7], 11, v[6:7]
	v_lshl_add_u64 v[6:7], v[4:5], 0, v[6:7]
	s_waitcnt lgkmcnt(0)
	global_store_dwordx4 v[6:7], v[20:23], off nt

.LBB0_1459:
	s_cmpk_lg_i32 s94, 0x100
	s_cselect_b64 s[4:5], -1, 0
	s_cmpk_lt_i32 s90, 0x60
	s_cselect_b64 s[6:7], -1, 0
	s_or_b64 s[4:5], s[6:7], s[4:5]
	s_and_b64 vcc, exec, s[4:5]
	s_cbranch_vccnz .LBB0_1518
	s_add_u32 s2, s84, 0x14b00000
	s_mul_i32 s5, s91, 0x2400
	s_addc_u32 s8, s85, 0
	s_add_i32 s5, s5, 0
	s_waitcnt vmcnt(0)
	v_and_b32_e32 v2, 7, v0
	s_mul_i32 s4, s90, 48
	v_mul_u32_u24_e32 v4, 0x90, v1
	v_lshrrev_b32_e32 v8, 3, v1
	v_lshl_add_u32 v9, v2, 4, s5
	v_lshlrev_b32_e32 v2, 3, v2
	s_add_u32 s10, s84, 0x4b00000
	s_mov_b32 s9, 0
	v_mov_b32_e32 v3, 0
	v_mul_u32_u24_e32 v10, 0x90, v8
	v_or_b32_e32 v11, 8, v8
	v_or_b32_e32 v12, 16, v8
	v_or_b32_e32 v13, 24, v8
	v_or_b32_e32 v14, 32, v8
	v_or_b32_e32 v15, 40, v8
	v_or_b32_e32 v16, 48, v8
	v_or_b32_e32 v17, 56, v8
	s_addc_u32 s11, s85, 0
	s_add_i32 s12, s91, s4
	s_addk_i32 s12, 0xf760
	s_movk_i32 s13, 0x4000
	s_movk_i32 s14, 0x800
	s_movk_i32 s15, 0x2000
	s_movk_i32 s16, 0x6000
	s_mov_b32 s17, 0xa000
	s_mov_b32 s18, 0x8000
	s_mov_b32 s19, 0xe000
	s_mov_b32 s20, 0xc000
	s_mov_b32 s21, 0x12000
	s_mov_b32 s22, 0x10000
	s_mov_b32 s23, 0x16000
	s_mov_b32 s24, 0x14000
	s_mov_b32 s25, 0x1a000
	s_mov_b32 s26, 0x18000
	s_mov_b32 s27, 0x1e000
	s_mov_b32 s28, 0x1c000
	s_mov_b32 s29, 0x22000
	s_mov_b32 s30, 0x20000
	s_mov_b32 s31, 0x26000
	s_mov_b32 s33, 0x24000
	s_mov_b32 s34, 0x2a000
	s_mov_b32 s35, 0x28000
	s_mov_b32 s36, 0x2e000
	s_mov_b32 s37, 0x2c000
	s_mov_b32 s38, 0x32000
	s_mov_b32 s39, 0x30000
	s_mov_b32 s40, 0x36000
	s_mov_b32 s41, 0x34000
	s_mov_b32 s42, 0x3a000
	s_mov_b32 s43, 0x38000
	s_mov_b32 s44, 0x3e000
	s_mov_b32 s45, 0x3c000
	s_mov_b32 s47, 0x60000
	s_mov_b32 s48, 0x66000
	s_mov_b32 s49, 0x64000
	s_mov_b32 s50, 0x6a000
	s_mov_b32 s51, 0x68000
	s_mov_b32 s52, 0x6e000
	s_mov_b32 s53, 0x6c000
	s_mov_b32 s54, 0x72000
	s_mov_b32 s55, 0x70000
	s_mov_b32 s56, 0x76000
	s_mov_b32 s57, 0x74000
	s_mov_b32 s58, 0x7a000
	s_mov_b32 s59, 0x78000
	s_mov_b32 s68, 0x7e000
	s_mov_b32 s69, 0x7c000
	v_add_u32_e32 v18, s5, v4
	s_movk_i32 s70, 0x400
	s_mov_b32 s71, 0x3f000
	v_lshlrev_b32_e32 v2, 1, v2
	s_branch .LBB0_1463
